# sb_phase (P4): XCD-aware query-block assignment, qb = 4*(unit&7) + ((unit>>3)&3): workgroups of one XCD take neighbouring query blocks so the previous key block is fetched by a neighbour into the same
# baseline (speedup 1.0000x reference)
; #define LAS __attribute__((address_space(3)))
; #define GAS __attribute__((address_space(1)))
; #define LAS __attribute__((address_space(3)))
; DI void sb_phase(LAS unsigned char* lds, const bf16* PROJ, bf16* MIX, const float* rsb, const float* gout, int bx, int G, int tid) {
;     ...
;     for (int unit = bx; unit < 1024; unit += G) {
;         const int qb = unit & 31, hd = (unit >> 5) & 15, b = unit >> 9;
;         const size_t m0 = (size_t)b * SEQ + 256 * qb, qrow = m0 + 32 * w + r;
;         const int tq = 256 * qb + 32 * w + r, D = 8 * qb + w;
;         const bf16* Kb = PROJ + ((size_t)b * SEQ) * INW + C_SK + 128 * hd; const bf16* Vb = PROJ + ((size_t)b * SEQ) * INW + C_SV + 128 * hd;
;         const float* rsk = rsb + ((size_t)32 + b * 16 + hd) * SEQ;
;         __syncthreads();
; #pragma unroll
;         for (int i = 0; i < 8; ++i) { const int sub = 8 * qb + i; const v4u v = *(const GAS v4u*)(Vb + (size_t)(32 * sub + (tid >> 4)) * INW + (tid & 15) * 8);
;             *(LAS v4u*)(VR + (sub % 9) * SLOT + (tid >> 4) * VSTR + (tid & 15) * 16) = v; }
;         bf16x8 qf[8]; load_qf(qf, PROJ + qrow * INW + C_SQ + 128 * hd, h);
;         const float qscale = rsb[((size_t)b * 16 + hd) * SEQ + tq] * (0.08838834764831845f * 1.4426950408889634f);
;         bf16x8 kf[8];
; #pragma unroll
;         for (int ks = 0; ks < 8; ++ks) kf[ks] = *(const GAS bf16x8*)(Kb + (size_t)(32 * D + r) * INW + 16 * ks + 8 * h);
;         v4u vnext = {0u, 0u, 0u, 0u};
;         if (qb > 0) vnext = *(const GAS v4u*)(Vb + (size_t)(32 * (8 * qb - 1) + (tid >> 4)) * INW + (tid & 15) * 8);
.LBB0_527:
	s_bfe_u32 s12, s33, 0x20003
	s_and_b32 s4, s33, 7
	s_lshl_b32 s4, s4, 2
	s_or_b32 s12, s12, s4
	s_ashr_i32 s4, s33, 9
	s_ashr_i32 s5, s4, 31
	s_lshl_b32 s13, s12, 8
	s_lshl_b64 s[8:9], s[4:5], 13
	v_add_u32_e32 v2, s13, v193
	s_bfe_u32 s90, s33, 0x40005
	v_lshl_add_u64 v[182:183], s[8:9], 0, v[2:3]
	s_lshl_b32 s14, s12, 3
	s_mul_i32 s9, s4, 0xe000000
	s_mul_hi_i32 s8, s4, 0xe000000
	s_add_u32 s9, s42, s9
	s_addc_u32 s8, s43, s8
	s_lshl_b32 s96, s90, 8
	s_add_u32 s10, s9, s96
	s_addc_u32 s11, s8, 0
	s_add_u32 s8, s10, 0x6000
	s_addc_u32 s9, s11, 0
	s_or_b32 s16, s14, 1
	s_mul_i32 s17, s16, 57
	s_lshr_b32 s17, s17, 9
	s_mul_i32 s17, s17, 9
	v_lshl_or_b32 v8, s16, 5, v194
	s_sub_i32 s16, s16, s17
	s_and_b32 s18, s16, 0xff
	s_or_b32 s16, s14, 2
	s_mul_i32 s17, s16, 57
	s_lshr_b32 s17, s17, 9
	s_mul_i32 s17, s17, 9
	v_lshl_or_b32 v14, s16, 5, v194
	s_sub_i32 s16, s16, s17
	s_and_b32 s19, s16, 0xff
	s_or_b32 s16, s14, 3
	s_mul_i32 s17, s16, 57
	s_lshr_b32 s17, s17, 9
	s_mul_i32 s17, s17, 9
	v_lshl_or_b32 v16, s16, 5, v194
	s_sub_i32 s16, s16, s17
	s_and_b32 s20, s16, 0xff
	s_or_b32 s16, s14, 4
	s_mul_i32 s17, s16, 57
	s_lshr_b32 s17, s17, 9
	s_mul_i32 s17, s17, 9
	v_lshl_or_b32 v22, s16, 5, v194
	s_sub_i32 s16, s16, s17
	s_and_b32 s21, s16, 0xff
	s_or_b32 s16, s14, 5
	s_mul_i32 s17, s16, 57
	s_lshr_b32 s17, s17, 9
	s_mul_i32 s17, s17, 9
	v_lshl_or_b32 v24, s16, 5, v194
	s_sub_i32 s16, s16, s17
	s_and_b32 s22, s16, 0xff
	s_or_b32 s16, s14, 6
	s_mul_i32 s17, s16, 57
	s_lshr_b32 s17, s17, 9
	s_mul_i32 s17, s17, 9
	v_lshl_or_b32 v30, s16, 5, v194
	s_sub_i32 s16, s16, s17
	s_and_b32 s23, s16, 0xff
	s_or_b32 s16, s14, 7
	v_or_b32_e32 v6, s13, v194
	v_lshl_or_b32 v32, s16, 5, v194
	v_mov_b32_e32 v177, v3
	v_mul_u32_u24_e32 v6, 0x3800, v6
	v_mul_u32_u24_e32 v8, 0x3800, v8
	v_mul_u32_u24_e32 v14, 0x3800, v14
	v_mul_u32_u24_e32 v16, 0x3800, v16
	v_mul_u32_u24_e32 v22, 0x3800, v22
	v_mul_u32_u24_e32 v24, 0x3800, v24
	v_mul_u32_u24_e32 v30, 0x3800, v30
	v_mul_u32_u24_e32 v32, 0x3800, v32
	s_mul_i32 s17, s16, 57
	v_lshl_add_u64 v[4:5], s[8:9], 0, v[176:177]
	v_lshlrev_b32_e32 v6, 1, v6
	v_mov_b32_e32 v7, v3
	v_lshlrev_b32_e32 v8, 1, v8
	v_mov_b32_e32 v9, v3
	v_lshlrev_b32_e32 v14, 1, v14
	v_mov_b32_e32 v15, v3
	v_lshlrev_b32_e32 v16, 1, v16
	v_mov_b32_e32 v17, v3
	v_lshlrev_b32_e32 v22, 1, v22
	v_mov_b32_e32 v23, v3
	v_lshlrev_b32_e32 v24, 1, v24
	v_mov_b32_e32 v25, v3
	v_lshlrev_b32_e32 v30, 1, v30
	v_mov_b32_e32 v31, v3
	v_lshlrev_b32_e32 v32, 1, v32
	v_mov_b32_e32 v33, v3
	s_lshr_b32 s17, s17, 9
	v_lshl_add_u64 v[6:7], v[4:5], 0, v[6:7]
	v_lshl_add_u64 v[10:11], v[4:5], 0, v[8:9]
	v_lshl_add_u64 v[14:15], v[4:5], 0, v[14:15]
	v_lshl_add_u64 v[18:19], v[4:5], 0, v[16:17]
	v_lshl_add_u64 v[22:23], v[4:5], 0, v[22:23]
	s_waitcnt vmcnt(0)
	v_lshl_add_u64 v[26:27], v[4:5], 0, v[24:25]
	v_lshl_add_u64 v[30:31], v[4:5], 0, v[30:31]
	v_lshl_add_u64 v[4:5], v[4:5], 0, v[32:33]
	s_mul_i32 s17, s17, 9
	s_waitcnt lgkmcnt(0)
	s_barrier
	s_mul_i32 s15, s12, 0x1c8
	global_load_dwordx4 v[6:9], v[6:7], off
	s_nop 0
	global_load_dwordx4 v[10:13], v[10:11], off
	s_nop 0
	global_load_dwordx4 v[14:17], v[14:15], off
	s_nop 0
	global_load_dwordx4 v[18:21], v[18:19], off
	s_nop 0
	global_load_dwordx4 v[22:25], v[22:23], off
	s_nop 0
	global_load_dwordx4 v[26:29], v[26:27], off
	s_nop 0
	global_load_dwordx4 v[30:33], v[30:31], off
	s_nop 0
	global_load_dwordx4 v[34:37], v[4:5], off
	s_sub_i32 s16, s16, s17
	v_mov_b64_e32 v[4:5], s[42:43]
	s_lshr_b32 s15, s15, 9
	s_and_b32 s24, s16, 0xff
	v_mad_u64_u32 v[4:5], s[16:17], v182, s88, v[4:5]
	s_mul_i32 s15, s15, 9
	v_mad_i32_i24 v5, v183, s88, v5
	s_sub_i32 s15, s14, s15
	v_lshl_add_u64 v[4:5], v[4:5], 0, s[96:97]
	v_mov_b32_e32 v179, v3
	s_and_b32 s15, s15, 0xff
	s_add_i32 s52, s14, s3
	v_lshl_add_u64 v[4:5], v[4:5], 0, v[178:179]
	s_mov_b64 s[16:17], 0x1000
	s_add_u32 s10, s10, 0x5000
	v_lshl_add_u64 v[38:39], v[4:5], 0, s[16:17]
	s_movk_i32 s16, 0x1000
	s_addc_u32 s11, s11, 0
	v_add_co_u32_e32 v4, vcc, s16, v4
	s_lshl_b64 s[16:17], s[4:5], 19
	s_add_u32 s5, s50, s16
	s_addc_u32 s17, s51, s17
	s_lshl_b32 s16, s90, 15
	s_add_u32 s16, s5, s16
	s_addc_u32 s17, s17, 0
	s_lshl_b32 s96, s52, 5
	v_addc_co_u32_e32 v5, vcc, 0, v5, vcc
	global_load_dwordx4 v[98:101], v[38:39], off offset:32
	global_load_dwordx4 v[102:105], v[38:39], off offset:64
	global_load_dwordx4 v[106:109], v[38:39], off offset:96
	global_load_dwordx4 v[110:113], v[38:39], off offset:128
	global_load_dwordx4 v[114:117], v[38:39], off offset:160
	global_load_dwordx4 v[118:121], v[38:39], off offset:192
	global_load_dwordx4 v[122:125], v[4:5], off
	global_load_dwordx4 v[126:129], v[38:39], off offset:224
	v_or_b32_e32 v40, s96, v171
	v_mov_b64_e32 v[38:39], s[10:11]
	v_lshl_add_u64 v[4:5], v[2:3], 2, s[16:17]
	v_mad_u64_u32 v[38:39], s[16:17], v40, s88, v[38:39]
	v_lshl_add_u64 v[38:39], v[38:39], 0, v[178:179]
	global_load_dword v4, v[4:5], off
	s_nop 0
	global_load_dwordx4 v[82:85], v[38:39], off
	global_load_dwordx4 v[158:161], v[38:39], off offset:32
	global_load_dwordx4 v[154:157], v[38:39], off offset:64
	global_load_dwordx4 v[150:153], v[38:39], off offset:96
	global_load_dwordx4 v[146:149], v[38:39], off offset:128
	global_load_dwordx4 v[142:145], v[38:39], off offset:160
	global_load_dwordx4 v[138:141], v[38:39], off offset:192
	global_load_dwordx4 v[134:137], v[38:39], off offset:224
	s_mulk_i32 s15, 0x2800
	v_add_u32_e32 v5, s15, v195
	s_mulk_i32 s18, 0x2800
	s_mulk_i32 s19, 0x2800
	s_mulk_i32 s20, 0x2800
	s_mulk_i32 s21, 0x2800
	s_mulk_i32 s22, 0x2800
	s_mulk_i32 s23, 0x2800
	s_mulk_i32 s24, 0x2800
	s_cmp_eq_u32 s12, 0
	s_waitcnt vmcnt(24)
	ds_write_b128 v5, v[6:9]
	v_add_u32_e32 v5, s18, v195
	s_waitcnt vmcnt(23)
	ds_write_b128 v5, v[10:13]
	v_add_u32_e32 v5, s19, v195
	s_waitcnt vmcnt(22)
	ds_write_b128 v5, v[14:17]
	v_add_u32_e32 v5, s20, v195
	s_waitcnt vmcnt(21)
	ds_write_b128 v5, v[18:21]
	v_add_u32_e32 v5, s21, v195
	s_waitcnt vmcnt(20)
	ds_write_b128 v5, v[22:25]
	v_add_u32_e32 v5, s22, v195
	s_waitcnt vmcnt(19)
	ds_write_b128 v5, v[26:29]
	v_add_u32_e32 v5, s23, v195
	s_waitcnt vmcnt(18)
	ds_write_b128 v5, v[30:33]
	v_add_u32_e32 v5, s24, v195
	s_waitcnt vmcnt(17)
	ds_write_b128 v5, v[34:37]
	s_cbranch_scc1 .LBB0_544
	v_add_u32_e32 v5, s13, v196
	v_mul_i32_i24_e32 v6, 0x3800, v5
	v_ashrrev_i32_e32 v7, 31, v6
	v_lshl_add_u64 v[6:7], v[6:7], 1, s[8:9]
	v_mov_b32_e32 v181, v3
	v_lshl_add_u64 v[6:7], v[6:7], 0, v[180:181]
	global_load_dwordx4 v[130:133], v[6:7], off
	s_and_saveexec_b64 s[12:13], s[6:7]

; #define LAS __attribute__((address_space(3)))
; #define GAS __attribute__((address_space(1)))
; #define LAS __attribute__((address_space(3)))
; DI void sb_phase(LAS unsigned char* lds, const bf16* PROJ, bf16* MIX, const float* rsb, const float* gout, int bx, int G, int tid) {
;     ...
;         float R = 0.f; bool wdone = false;
;         for (int s = 0; ; ++s) {
;             const int sub = D - s;
;             if (sub < 0) wdone = true;
;             LAS unsigned* F = FL + 8 * (s & 1);
;             if (lane == 0) F[w] = wdone ? 1u : 0u;
;             if (s > 0 && 8 * qb - s >= 0) *(LAS v4u*)(VR + ((8 * qb - s) % 9) * SLOT + (tid >> 4) * VSTR + (tid & 15) * 16) = vnext;
;             __syncthreads();
;             { const unsigned all = F[0] & F[1] & F[2] & F[3] & F[4] & F[5] & F[6] & F[7]; if (all) break; }
;             { const int subv = 8 * qb - s - 1 >= 0 ? 8 * qb - s - 1 : 0; vnext = *(const GAS v4u*)(Vb + (size_t)(32 * subv + (tid >> 4)) * INW + (tid & 15) * 8); }
.LBB0_532:
	s_bfe_u32 s8, s47, 0x20003
	s_and_b32 s9, s47, 7
	s_lshl_b32 s9, s9, 2
	s_or_b32 s8, s8, s9
	s_lshl_b32 s9, s8, 3
	s_mul_i32 s13, s8, 0x14000
	s_add_i32 s14, s87, s9
	s_add_i32 s12, s9, -1
	s_addk_i32 s13, 0xd800
	s_lshl_b32 s96, s14, 5
	s_mov_b32 s15, 8
	v_mov_b32_e32 v2, v225
	v_mov_b32_e32 v16, v198
	s_branch .LBB0_535
